# deferred weight-conversion split: all layer-1 tiles deferred, idle-slot quotas 8/12/12/14
# speedup vs baseline: 1.0063x; 1.0063x over previous
; #define SEAM(k) do { if (IN(k) && IN((k) + 1)) xcd_barrier(bar); \
;         if (PROBE_MASK) { const unsigned long long t_ = __builtin_amdgcn_s_memrealtime(); if ((PROBE_MASK >> (k)) & 1u) pr_acc += t_ - pr_t0; pr_t0 = t_; } } while (0)
; __device__ __forceinline__ void convert_deferred(const Ptrs& P, unsigned char* lds, int quota) {
;     const int tid = threadIdx.x, wid = tid >> 6, lane = tid & 63;
;     float* tile = (float*)lds;
;     volatile __attribute__((address_space(3))) int* slot = (volatile __attribute__((address_space(3))) int*)((__attribute__((address_space(3))) unsigned char*)lds + 131072 + 320 + 11000);
;     unsigned* q = (unsigned*)(P.ws + WS_CTL) + CW_DEFQ;
;     for (int n = 0; n < quota; ++n) {
;         __syncthreads();
;         if (tid == 0) *slot = (int)atomicAdd(q, 1u);
;         __syncthreads();
;         const int t = *slot;
;         if (t >= DEF_GU + DEF_DN) break;
;         const bool gu = t < DEF_GU;
;         const float* src = gu ? P.in[34] : P.in[36]; bf16* dst = (bf16*)(P.ws + (gu ? WS_WGU : WS_WDN));
;         const int N = gu ? 2048 : 1024, ntn = N / 256, it = gu ? 2 * NE * 16 * 8 - DEF_GU + t : 2 * NE * 16 * 4 - DEF_DN + (t - DEF_GU);
; __global__ void __launch_bounds__(NT, 2) mega(Args args) {
;     ...
;         if (IDLE_LAST(68 * 7)) convert_deferred(P, lds, 4); } SEAM(2);
.LBB0_779:
	s_abs_i32 s3, s62
	v_cvt_f32_u32_e32 v2, s3
	s_sub_i32 s4, 0, s3
	s_mov_b32 s5, 0
	v_rcp_iflag_f32_e32 v2, v2
	s_nop 0
	v_mul_f32_e32 v2, 0x4f7ffffe, v2
	v_cvt_u32_f32_e32 v2, v2
	s_nop 0
	v_readfirstlane_b32 s6, v2
	s_mul_i32 s4, s4, s6
	s_mul_hi_u32 s4, s6, s4
	s_add_i32 s6, s6, s4
	s_mul_hi_u32 s4, s6, 0x1dc
	s_mul_i32 s4, s4, s3
	s_sub_i32 s4, 0x1dc, s4
	s_sub_i32 s6, s4, s3
	s_cmp_ge_u32 s4, s3
	s_cselect_b32 s4, s6, s4
	s_sub_i32 s6, s4, s3
	s_cmp_ge_u32 s4, s3
	s_cselect_b32 s3, s6, s4
	s_cmp_eq_u32 s3, 0
	s_cselect_b64 s[6:7], -1, 0
	s_cmp_lt_i32 s2, s3
	s_cselect_b64 s[8:9], -1, 0
	s_or_b64 s[6:7], s[6:7], s[8:9]
	s_and_b64 vcc, exec, s[6:7]
	s_cbranch_vccnz .LBB0_789
	v_and_b32_e32 v2, 0x7c, v155
	v_lshlrev_b32_e32 v3, 5, v0
	s_movk_i32 s3, 0x400
	v_lshrrev_b32_e32 v4, 6, v0
	v_and_or_b32 v12, v3, s3, v2
	v_bfe_u32 v2, v0, 3, 3
	v_lshl_or_b32 v5, v4, 5, v2
	v_lshlrev_b32_e32 v2, 3, v0
	v_lshl_add_u32 v11, v182, 4, 0
	v_and_b32_e32 v2, 56, v2
	v_mul_u32_u24_e32 v16, 0x2020, v4
	v_mov_b32_e32 v3, 0
	v_lshl_add_u32 v27, v5, 2, 0
	v_mul_u32_u24_e32 v28, 0x404, v2
	v_lshlrev_b32_e32 v10, 6, v5
	s_add_i32 s12, 0, 0x22c38
	v_add_u32_e32 v16, v11, v16
	v_and_b32_e32 v13, 0xfc, v155
	v_and_b32_e32 v14, 56, v154
	s_mov_b32 s3, 8
	v_or_b32_e32 v4, 0x200, v10
	v_mov_b32_e32 v5, v3
	v_or_b32_e32 v6, 0x400, v10
	v_mov_b32_e32 v7, v3
	v_or_b32_e32 v8, 0x600, v10
	v_mov_b32_e32 v9, v3
	v_mov_b32_e32 v15, s12
	s_movk_i32 s13, 0x17ff
	s_movk_i32 s14, 0x800
	s_mov_b32 s15, 0x1104e000
	s_movk_i32 s16, -2048
	v_add_u32_e32 v17, 0x404, v16
	v_add_u32_e32 v18, 0x40c, v16
	v_add_u32_e32 v19, 0x808, v16
	v_add_u32_e32 v20, 0xc0c, v16
	v_add_u32_e32 v21, 0xc14, v16
	v_add_u32_e32 v22, 0x1414, v16
	v_add_u32_e32 v23, 0x141c, v16
	v_add_u32_e32 v24, 0x1818, v16
	v_add_u32_e32 v25, 0x1c1c, v16
	v_add_u32_e32 v26, 0x1c24, v16
	v_lshlrev_b32_e32 v2, 1, v2
	v_add_u32_e32 v27, v27, v28
	v_lshlrev_b32_e32 v10, 1, v10
	s_branch .LBB0_782

; #define SEAM(k) do { if (IN(k) && IN((k) + 1)) xcd_barrier(bar); \
;         if (PROBE_MASK) { const unsigned long long t_ = __builtin_amdgcn_s_memrealtime(); if ((PROBE_MASK >> (k)) & 1u) pr_acc += t_ - pr_t0; pr_t0 = t_; } } while (0)
; __device__ __forceinline__ void convert_deferred(const Ptrs& P, unsigned char* lds, int quota) {
;     const int tid = threadIdx.x, wid = tid >> 6, lane = tid & 63;
;     float* tile = (float*)lds;
;     volatile __attribute__((address_space(3))) int* slot = (volatile __attribute__((address_space(3))) int*)((__attribute__((address_space(3))) unsigned char*)lds + 131072 + 320 + 11000);
;     unsigned* q = (unsigned*)(P.ws + WS_CTL) + CW_DEFQ;
;     for (int n = 0; n < quota; ++n) {
;         __syncthreads();
;         if (tid == 0) *slot = (int)atomicAdd(q, 1u);
;         __syncthreads();
;         const int t = *slot;
;         if (t >= DEF_GU + DEF_DN) break;
;         const bool gu = t < DEF_GU;
;         const float* src = gu ? P.in[34] : P.in[36]; bf16* dst = (bf16*)(P.ws + (gu ? WS_WGU : WS_WDN));
;         const int N = gu ? 2048 : 1024, ntn = N / 256, it = gu ? 2 * NE * 16 * 8 - DEF_GU + t : 2 * NE * 16 * 4 - DEF_DN + (t - DEF_GU);
; __global__ void __launch_bounds__(NT, 2) mega(Args args) {
;     ...
;         if (IDLE_LAST(68 * 4)) convert_deferred(P, lds, 4); } SEAM(6);
.LBB0_1286:
	s_abs_i32 s3, s62
	v_cvt_f32_u32_e32 v2, s3
	s_sub_i32 s4, 0, s3
	s_mov_b32 s5, 0
	v_rcp_iflag_f32_e32 v2, v2
	s_nop 0
	v_mul_f32_e32 v2, 0x4f7ffffe, v2
	v_cvt_u32_f32_e32 v2, v2
	s_nop 0
	v_readfirstlane_b32 s6, v2
	s_mul_i32 s4, s4, s6
	s_mul_hi_u32 s4, s6, s4
	s_add_i32 s6, s6, s4
	s_mul_hi_u32 s4, s6, 0x110
	s_mul_i32 s4, s4, s3
	s_sub_i32 s4, 0x110, s4
	s_sub_i32 s6, s4, s3
	s_cmp_ge_u32 s4, s3
	s_cselect_b32 s4, s6, s4
	s_sub_i32 s6, s4, s3
	s_cmp_ge_u32 s4, s3
	s_cselect_b32 s3, s6, s4
	s_cmp_eq_u32 s3, 0
	s_cselect_b64 s[6:7], -1, 0
	s_cmp_lt_i32 s2, s3
	s_cselect_b64 s[8:9], -1, 0
	s_or_b64 s[6:7], s[6:7], s[8:9]
	s_and_b64 vcc, exec, s[6:7]
	s_cbranch_vccnz .LBB0_1296
	v_and_b32_e32 v2, 0x7c, v188
	v_lshlrev_b32_e32 v3, 5, v0
	s_movk_i32 s3, 0x400
	v_and_or_b32 v12, v3, s3, v2
	v_bfe_u32 v2, v0, 3, 3
	v_lshl_or_b32 v4, v1, 5, v2
	v_lshlrev_b32_e32 v2, 3, v0
	v_lshl_add_u32 v11, v182, 4, 0
	v_and_b32_e32 v2, 56, v2
	v_mul_u32_u24_e32 v16, 0x2020, v1
	v_mov_b32_e32 v3, 0
	v_lshl_add_u32 v27, v4, 2, 0
	v_mul_u32_u24_e32 v28, 0x404, v2
	v_lshlrev_b32_e32 v10, 6, v4
	s_add_i32 s12, 0, 0x22c38
	v_add_u32_e32 v16, v11, v16
	v_and_b32_e32 v13, 0xfc, v188
	v_and_b32_e32 v14, 56, v185
	s_mov_b32 s3, 12
	v_or_b32_e32 v4, 0x200, v10
	v_mov_b32_e32 v5, v3
	v_or_b32_e32 v6, 0x400, v10
	v_mov_b32_e32 v7, v3
	v_or_b32_e32 v8, 0x600, v10
	v_mov_b32_e32 v9, v3
	v_mov_b32_e32 v15, s12
	s_movk_i32 s13, 0x17ff
	s_movk_i32 s14, 0x800
	s_mov_b32 s15, 0x1104e000
	s_movk_i32 s16, -2048
	v_add_u32_e32 v17, 0x404, v16
	v_add_u32_e32 v18, 0x40c, v16
	v_add_u32_e32 v19, 0x808, v16
	v_add_u32_e32 v20, 0xc0c, v16
	v_add_u32_e32 v21, 0xc14, v16
	v_add_u32_e32 v22, 0x1414, v16
	v_add_u32_e32 v23, 0x141c, v16
	v_add_u32_e32 v24, 0x1818, v16
	v_add_u32_e32 v25, 0x1c1c, v16
	v_add_u32_e32 v26, 0x1c24, v16
	v_lshlrev_b32_e32 v2, 1, v2
	v_add_u32_e32 v27, v27, v28
	v_lshlrev_b32_e32 v10, 1, v10
	s_branch .LBB0_1289

; #define LAS __attribute__((address_space(3)))
; #define SEAM(k) do { if (IN(k) && IN((k) + 1)) xcd_barrier(bar); \
;         if (PROBE_MASK) { const unsigned long long t_ = __builtin_amdgcn_s_memrealtime(); if ((PROBE_MASK >> (k)) & 1u) pr_acc += t_ - pr_t0; pr_t0 = t_; } } while (0)
; __device__ __forceinline__ void convert_deferred(const Ptrs& P, unsigned char* lds, int quota) {
;     const int tid = threadIdx.x, wid = tid >> 6, lane = tid & 63;
;     float* tile = (float*)lds;
;     volatile __attribute__((address_space(3))) int* slot = (volatile __attribute__((address_space(3))) int*)((__attribute__((address_space(3))) unsigned char*)lds + 131072 + 320 + 11000);
;     unsigned* q = (unsigned*)(P.ws + WS_CTL) + CW_DEFQ;
;     for (int n = 0; n < quota; ++n) {
;         __syncthreads();
;         if (tid == 0) *slot = (int)atomicAdd(q, 1u);
;         __syncthreads();
;         const int t = *slot;
;         if (t >= DEF_GU + DEF_DN) break;
;         const bool gu = t < DEF_GU;
;         const float* src = gu ? P.in[34] : P.in[36]; bf16* dst = (bf16*)(P.ws + (gu ? WS_WGU : WS_WDN));
;         const int N = gu ? 2048 : 1024, ntn = N / 256, it = gu ? 2 * NE * 16 * 8 - DEF_GU + t : 2 * NE * 16 * 4 - DEF_DN + (t - DEF_GU);
; __global__ void __launch_bounds__(NT, 2) mega(Args args) {
;     ...
;         { const int rem_ = ((LAS int*)(LDSP + MISC_OFF + 256))[96] % G; if (rem_ != 0 && vcu >= rem_) convert_deferred(P, lds, 5); } } SEAM(9);
.LBB0_1609:
	s_abs_i32 s0, s62
	v_cvt_f32_u32_e32 v2, s0
	s_sub_i32 s5, 0, s0
	s_abs_i32 s4, s9
	s_ashr_i32 s3, s9, 31
	v_rcp_iflag_f32_e32 v2, v2
	s_mov_b32 s1, 0
	v_mul_f32_e32 v2, 0x4f7ffffe, v2
	v_cvt_u32_f32_e32 v2, v2
	s_nop 0
	v_readfirstlane_b32 s6, v2
	s_mul_i32 s5, s5, s6
	s_mul_hi_u32 s5, s6, s5
	s_add_i32 s6, s6, s5
	s_mul_hi_u32 s5, s4, s6
	s_mul_i32 s5, s5, s0
	s_sub_i32 s4, s4, s5
	s_sub_i32 s5, s4, s0
	s_cmp_ge_u32 s4, s0
	s_cselect_b32 s4, s5, s4
	s_sub_i32 s5, s4, s0
	s_cmp_ge_u32 s4, s0
	s_cselect_b32 s0, s5, s4
	s_xor_b32 s0, s0, s3
	s_sub_i32 s0, s0, s3
	s_cmp_eq_u32 s0, 0
	v_readlane_b32 s3, v254, 2
	s_cselect_b64 s[4:5], -1, 0
	s_cmp_lt_i32 s3, s0
	s_cselect_b64 s[6:7], -1, 0
	s_or_b64 s[4:5], s[4:5], s[6:7]
	s_and_b64 vcc, exec, s[4:5]
	s_cbranch_vccnz .LBB0_1619
	v_and_b32_e32 v2, 0x7c, v175
	v_lshlrev_b32_e32 v3, 5, v0
	s_movk_i32 s0, 0x400
	v_and_or_b32 v12, v3, s0, v2
	v_bfe_u32 v2, v0, 3, 3
	v_lshl_or_b32 v4, v1, 5, v2
	v_lshlrev_b32_e32 v2, 3, v0
	v_lshl_add_u32 v11, v182, 4, 0
	v_and_b32_e32 v2, 56, v2
	v_mul_u32_u24_e32 v16, 0x2020, v1
	v_mov_b32_e32 v3, 0
	v_lshl_add_u32 v27, v4, 2, 0
	v_mul_u32_u24_e32 v28, 0x404, v2
	v_lshlrev_b32_e32 v10, 6, v4
	s_add_i32 s10, 0, 0x22c38
	v_add_u32_e32 v16, v11, v16
	s_mov_b32 s3, 12
	v_and_b32_e32 v13, 0xfc, v175
	v_and_b32_e32 v14, 56, v173
	v_or_b32_e32 v4, 0x200, v10
	v_mov_b32_e32 v5, v3
	v_or_b32_e32 v6, 0x400, v10
	v_mov_b32_e32 v7, v3
	v_or_b32_e32 v8, 0x600, v10
	v_mov_b32_e32 v9, v3
	v_mov_b32_e32 v15, s10
	s_movk_i32 s11, 0x17ff
	s_movk_i32 s12, 0x800
	s_mov_b32 s13, 0x1104e000
	s_movk_i32 s14, -2048
	v_add_u32_e32 v17, 0x404, v16
	v_add_u32_e32 v18, 0x40c, v16
	v_add_u32_e32 v19, 0x808, v16
	v_add_u32_e32 v20, 0xc0c, v16
	v_add_u32_e32 v21, 0xc14, v16
	v_add_u32_e32 v22, 0x1414, v16
	v_add_u32_e32 v23, 0x141c, v16
	v_add_u32_e32 v24, 0x1818, v16
	v_add_u32_e32 v25, 0x1c1c, v16
	v_add_u32_e32 v26, 0x1c24, v16
	v_lshlrev_b32_e32 v2, 1, v2
	v_add_u32_e32 v27, v27, v28
	v_lshlrev_b32_e32 v10, 1, v10
	s_branch .LBB0_1612

; #define SEAM(k) do { if (IN(k) && IN((k) + 1)) xcd_barrier(bar); \
;         if (PROBE_MASK) { const unsigned long long t_ = __builtin_amdgcn_s_memrealtime(); if ((PROBE_MASK >> (k)) & 1u) pr_acc += t_ - pr_t0; pr_t0 = t_; } } while (0)
; __device__ __forceinline__ void convert_deferred(const Ptrs& P, unsigned char* lds, int quota) {
;     const int tid = threadIdx.x, wid = tid >> 6, lane = tid & 63;
;     float* tile = (float*)lds;
;     volatile __attribute__((address_space(3))) int* slot = (volatile __attribute__((address_space(3))) int*)((__attribute__((address_space(3))) unsigned char*)lds + 131072 + 320 + 11000);
;     unsigned* q = (unsigned*)(P.ws + WS_CTL) + CW_DEFQ;
;     for (int n = 0; n < quota; ++n) {
;         __syncthreads();
;         if (tid == 0) *slot = (int)atomicAdd(q, 1u);
;         __syncthreads();
;         const int t = *slot;
;         if (t >= DEF_GU + DEF_DN) break;
;         const bool gu = t < DEF_GU;
;         const float* src = gu ? P.in[34] : P.in[36]; bf16* dst = (bf16*)(P.ws + (gu ? WS_WGU : WS_WDN));
;         const int N = gu ? 2048 : 1024, ntn = N / 256, it = gu ? 2 * NE * 16 * 8 - DEF_GU + t : 2 * NE * 16 * 4 - DEF_DN + (t - DEF_GU);
; __global__ void __launch_bounds__(NT, 2) mega(Args args) {
;     ...
;         if (IDLE_LAST(68 * 12)) convert_deferred(P, lds, 4); } SEAM(11);
.LBB0_1851:
	s_abs_i32 s0, s62
	v_cvt_f32_u32_e32 v2, s0
	s_sub_i32 s3, 0, s0
	v_readlane_b32 s56, v254, 40
	s_mov_b32 s1, 0
	v_rcp_iflag_f32_e32 v2, v2
	v_readlane_b32 s57, v254, 41
	v_mul_f32_e32 v2, 0x4f7ffffe, v2
	v_cvt_u32_f32_e32 v2, v2
	s_nop 0
	v_readfirstlane_b32 s4, v2
	s_mul_i32 s3, s3, s4
	s_mul_hi_u32 s3, s4, s3
	s_add_i32 s4, s4, s3
	s_mul_hi_u32 s3, s4, 0x330
	s_mul_i32 s3, s3, s0
	s_sub_i32 s3, 0x330, s3
	s_sub_i32 s4, s3, s0
	s_cmp_ge_u32 s3, s0
	s_cselect_b32 s3, s4, s3
	s_sub_i32 s4, s3, s0
	s_cmp_ge_u32 s3, s0
	s_cselect_b32 s0, s4, s3
	s_cmp_eq_u32 s0, 0
	s_cselect_b64 s[4:5], -1, 0
	s_cmp_lt_i32 s2, s0
	s_cselect_b64 s[6:7], -1, 0
	s_or_b64 s[4:5], s[4:5], s[6:7]
	s_and_b64 vcc, exec, s[4:5]
	s_cbranch_vccnz .LBB0_1861
	v_and_b32_e32 v2, 0x7c, v218
	v_lshlrev_b32_e32 v3, 5, v0
	s_movk_i32 s0, 0x400
	v_and_or_b32 v12, v3, s0, v2
	v_bfe_u32 v2, v0, 3, 3
	v_lshl_or_b32 v4, v1, 5, v2
	v_lshlrev_b32_e32 v2, 3, v0
	v_lshl_add_u32 v11, v182, 4, 0
	v_and_b32_e32 v2, 56, v2
	v_mul_u32_u24_e32 v16, 0x2020, v1
	v_mov_b32_e32 v3, 0
	s_waitcnt vmcnt(0)
	v_lshl_add_u32 v27, v4, 2, 0
	v_mul_u32_u24_e32 v28, 0x404, v2
	v_lshlrev_b32_e32 v10, 6, v4
	s_add_i32 s10, 0, 0x22c38
	v_add_u32_e32 v16, v11, v16
	v_and_b32_e32 v13, 0xfc, v218
	v_and_b32_e32 v14, 56, v179
	s_mov_b32 s3, 14
	v_or_b32_e32 v4, 0x200, v10
	v_mov_b32_e32 v5, v3
	v_or_b32_e32 v6, 0x400, v10
	v_mov_b32_e32 v7, v3
	v_or_b32_e32 v8, 0x600, v10
	v_mov_b32_e32 v9, v3
	v_mov_b32_e32 v15, s10
	s_movk_i32 s11, 0x17ff
	s_movk_i32 s12, 0x800
	s_mov_b32 s13, 0x1104e000
	s_movk_i32 s14, -2048
	v_add_u32_e32 v17, 0x404, v16
	v_add_u32_e32 v18, 0x40c, v16
	v_add_u32_e32 v19, 0x808, v16
	v_add_u32_e32 v20, 0xc0c, v16
	v_add_u32_e32 v21, 0xc14, v16
	v_add_u32_e32 v22, 0x1414, v16
	v_add_u32_e32 v23, 0x141c, v16
	v_add_u32_e32 v24, 0x1818, v16
	v_add_u32_e32 v25, 0x1c1c, v16
	v_add_u32_e32 v26, 0x1c24, v16
	v_lshlrev_b32_e32 v2, 1, v2
	v_add_u32_e32 v27, v27, v28
	v_lshlrev_b32_e32 v10, 1, v10
	s_branch .LBB0_1854
